# v70 with 1024 layer-1 down-projection conversion items shifted from the end of layer 0's down-projection phase into layer 1's in-projection slack (DN-end 3072 items, layer-1 in-projection 4608 items)
# speedup vs baseline: 1.0024x; 1.0024x over previous
; #define LAS __attribute__((address_space(3)))
; __device__ __forceinline__ int opaque_tid() { int t = threadIdx.x; asm volatile("" : "+v"(t)); return t; }
;     const int tid = opaque_tid(), lane = tid & 63, wave = tid >> 6;
;     LAS float* scr = (LAS float*)(lds + 49152) + wave * (64 * 33);
;     const int gw = ((int)blockIdx.x - blk0) * NWAVES + wave, ngw = nblk * NWAVES;
;     constexpr int I_L = 16 * 104 + 16 * 32 + 16 * 16 * 32 + 16 * 8 * 32;
;     if ((int)blockIdx.x < blk0 || (int)blockIdx.x >= blk0 + nblk) return;
;     float tv[32];
;     const int I_E = it_hi < I_L ? it_hi : I_L;
;     int it = it_lo + gw;
; __device__ __forceinline__ void pj_mfma(const Args& a, LAS unsigned char* lds, int layer) {
;     ...
;     if (layer + 1 < NL) { __syncthreads(); constexpr int I_SPLIT = 10240;
;         const int half = gridDim.x / 2; const bool upper = (int)blockIdx.x >= half;
;         p0_prep(a, lds, layer + 1, upper ? half : 0, upper ? (int)gridDim.x - half : half, upper ? 0 : I_SPLIT, upper ? I_SPLIT : (1 << 30)); }
.Lpj_l1_prep:
	s_lshr_b32 s4, s77, 1
	s_sub_i32 s5, s77, s4
	s_cmp_ge_u32 s61, s4
	s_cselect_b64 s[6:7], -1, 0
	s_sub_i32 s8, s61, s4
	s_lshl_b32 s8, s8, 3
	s_addk_i32 s8, 0x1a80
	s_lshl_b32 s5, s5, 3
	s_movk_i32 s9, 0x2c80
	s_nop 0
	v_writelane_b32 v252, s9, 36
	v_writelane_b32 v252, s5, 37
	v_writelane_b32 v252, s6, 38
	v_writelane_b32 v252, s7, 39
	v_writelane_b32 v252, s8, 40
	s_branch .Lprep_go

; #define LAS __attribute__((address_space(3)))
; __device__ __forceinline__ int opaque_tid() { int t = threadIdx.x; asm volatile("" : "+v"(t)); return t; }
;     const int tid = opaque_tid(), lane = tid & 63, wave = tid >> 6;
;     LAS float* scr = (LAS float*)(lds + 49152) + wave * (64 * 33);
;     const int gw = ((int)blockIdx.x - blk0) * NWAVES + wave, ngw = nblk * NWAVES;
;     constexpr int I_L = 16 * 104 + 16 * 32 + 16 * 16 * 32 + 16 * 8 * 32;
;     if ((int)blockIdx.x < blk0 || (int)blockIdx.x >= blk0 + nblk) return;
;     float tv[32];
;     const int I_E = it_hi < I_L ? it_hi : I_L;
;     int it = it_lo + gw;
;     if (it < I_E) { const PrepItem p = prep_decode(a, l, it);
; #pragma unroll
;         for (int i = 0; i < 32; ++i) tv[i] = __builtin_nontemporal_load(p.src + (size_t)(2 * i + (lane >> 5)) * p.ldw + (lane & 31)); }
; __device__ __forceinline__ void dn_mfma(const Args& a, LAS unsigned char* lds, int layer) {
;     seg_to_lds(a, lds, layer);
;     const LAS int* seg = (const LAS int*)(lds + SEG_OFF);
;     pg8::GroupedOrder So{(const char*)(a.ws + WS_HID), (const char*)(a.ws + WS_WDN + (size_t)layer * NE * 1024 * DFF * 2), seg, 4, (int)gridDim.x, (int)blockIdx.x, (size_t)DFF * 2, (size_t)1024 * DFF * 2, (size_t)256 * DFF * 2};
;     EpiDown E{(bf16_t*)(a.ws + WS_YBUF), (const int*)(a.ws + WS_LIST), (const float*)(a.ws + WS_LISTW), seg, lds};
;     pg8::gemm_phase<EpiDown, pg8::GroupedOrder>(lds, DFF, So, E);
; }
.LBB0_1321:
	v_readlane_b32 vcc_lo, v254, 16
	s_nop 1
	s_cmp_lg_u32 vcc_lo, 0
	s_cbranch_scc1 .Ldn_prep_skip
	v_readlane_b32 s4, v254, 63
	s_nop 1
	s_mul_i32 s4, s4, 3
	s_cmpk_eq_u32 s77, 0x100
	s_cselect_b32 s4, s4, 0
	s_sub_i32 s5, s77, s4
	s_cmp_ge_u32 s61, s4
	s_cselect_b64 s[6:7], -1, 0
	s_sub_i32 s8, s61, s4
	s_lshl_b32 s8, s8, 3
	s_addk_i32 s8, 0x2c80
	s_lshl_b32 s5, s5, 3
	s_movk_i32 s9, 0x3880
	s_mov_b32 s10, 1
	s_nop 0
	v_writelane_b32 v252, s9, 36
	v_writelane_b32 v252, s5, 37
	v_writelane_b32 v252, s6, 38
	v_writelane_b32 v252, s7, 39
	v_writelane_b32 v252, s8, 40
	v_writelane_b32 v254, s10, 60
	v_mov_b32_e32 v112, v57
	s_mov_b64 s[44:45], -1
	s_branch .LBB0_302
